# sel-attn units from an atomic work queue in descending-cost order (first ticket static) on top of combo3
# speedup vs baseline: 1.0033x; 1.0013x over previous
; __device__ __forceinline__ float bf2f(unsigned v) { return __uint_as_float(v << 16); }
; __device__ __forceinline__ unsigned pk2(float lo, float hi) { const f32x2 f = {lo, hi}; const bf16n2 v = __builtin_convertvector(f, bf16n2); return __builtin_bit_cast(unsigned, v); }
; __device__ __forceinline__ float sigmoidf_(float x) { return __builtin_amdgcn_rcpf(1.0f + __expf(-x)); }
; __device__ __forceinline__ f32x4 unpack4(u32x2 z) { return (f32x4){__uint_as_float(z.x << 16), __uint_as_float(z.x & 0xffff0000u), __uint_as_float(z.y << 16), __uint_as_float(z.y & 0xffff0000u)}; }
;     ...
;         for (int qd = 0; qd < NQ; ++qd) {
;             const int tq = tw0 + 4 * qd + (n >> 2), hh = g * 4 + hr;
;             f32x4 accp[4]; u32x2 winp[4];
;             if (MODE == 3) {
; #pragma unroll
;                 for (int dt = 0; dt < 4; ++dt) { const int col = hh * 64 + 16 * dt + 4 * q; accp[dt] = unpack4(*(const u32x2*)((const bf16_t*)nsaacc + (size_t)tq * 512 + col)); winp[dt] = *(const u32x2*)(oout + (size_t)tq * 512 + col); } }
;             float scale;
;             if (MODE == 2) scale = 1.0f;
;             else { float lt = lrun[qd]; lt += __shfl_xor(lt, 16); lt += __shfl_xor(lt, 32);
;                 if (MODE == 0) { const float sink = sinkv; const float mf = fmaxf(mrun[qd], sink), cr = __expf(mrun[qd] - mf); scale = cr / (lt * cr + __expf(sink - mf)); }
;                 else scale = lt > 0.f ? 1.0f / lt : 0.f; }
;             if (MODE != 0) scale *= sigmoidf_(bf2f(graw[qd]));
; #pragma unroll
;             for (int dt = 0; dt < 4; ++dt) { const f32x4 o = O[qd][dt] * scale; const int col = hh * 64 + 16 * dt + 4 * q;
;                 if (MODE == 0 || MODE == 1) { u32x2 w; w.x = pk2(o[0], o[1]); w.y = pk2(o[2], o[3]); *(u32x2*)(oout + (size_t)tq * 512 + col) = w; }
;                 else if (MODE == 2) { u32x2 w; w.x = pk2(o[0], o[1]); w.y = pk2(o[2], o[3]); *(u32x2*)((bf16_t*)nsaacc + (size_t)tq * 512 + col) = w; }
;                 else { const f32x4 t2 = (accp[dt] + unpack4(winp[dt])) + o; u32x2 w; w.x = pk2(t2[0], t2[1]); w.y = pk2(t2[2], t2[3]); *(u32x2*)(oout + (size_t)tq * 512 + col) = w; } }
;         }
.LBB0_1120:
	v_readlane_b32 s0, v254, 29
	v_readlane_b32 s1, v254, 27
	v_readlane_b32 s2, v252, 29
	v_readlane_b32 s3, v252, 30
	s_lshl_b32 s0, s0, 4
	s_or_b32 s0, s0, s1
	s_lshl_b32 s0, s0, 2
	s_add_u32 s2, s2, s0
	s_addc_u32 s3, s3, 0
	s_and_saveexec_b64 s[4:5], s[8:9]
	v_mov_b32_e32 v250, 1
	global_atomic_add v188, v1, v250, s[2:3] offset:512 sc0
	s_or_b64 exec, exec, s[4:5]
	v_or_b32_e32 v58, s12, v156
	v_lshl_or_b32 v58, v58, 6, v189
	v_readlane_b32 s0, v252, 25
	v_lshlrev_b64 v[62:63], 10, v[196:197]
	v_readlane_b32 s1, v252, 26
	v_ashrrev_i32_e32 v59, 31, v58
	v_lshlrev_b64 v[60:61], 1, v[58:59]
	v_lshl_add_u64 v[64:65], s[0:1], 0, v[62:63]
	v_lshl_add_u64 v[58:59], v[64:65], 0, v[60:61]
	global_load_dwordx2 v[66:67], v[58:59], off
	global_load_dwordx2 v[68:69], v[58:59], off offset:32
	global_load_dwordx2 v[70:71], v[58:59], off offset:64
	global_load_dwordx2 v[110:111], v[58:59], off offset:96
	v_lshl_add_u64 v[58:59], s[88:89], 0, v[62:63]
	v_lshl_add_u64 v[58:59], v[58:59], 0, v[60:61]
	v_lshlrev_b64 v[62:63], 10, v[184:185]
	global_load_dwordx2 v[108:109], v[58:59], off
	global_load_dwordx2 v[106:107], v[58:59], off offset:32
	global_load_dwordx2 v[72:73], v[58:59], off offset:64
	global_load_dwordx2 v[112:113], v[58:59], off offset:96
	v_lshl_add_u64 v[64:65], s[0:1], 0, v[62:63]
	v_lshl_add_u64 v[64:65], v[64:65], 0, v[60:61]
	global_load_dwordx2 v[118:119], v[64:65], off
	global_load_dwordx2 v[120:121], v[64:65], off offset:32
	global_load_dwordx2 v[114:115], v[64:65], off offset:64
	global_load_dwordx2 v[116:117], v[64:65], off offset:96
	ds_bpermute_b32 v123, v230, v203
	ds_bpermute_b32 v122, v230, v202
	v_lshlrev_b32_e32 v64, 16, v235
	v_lshl_add_u64 v[62:63], s[88:89], 0, v[62:63]
	v_mul_f32_e32 v64, 0xbfb8aa3b, v64
	v_lshl_add_u64 v[60:61], v[62:63], 0, v[60:61]
	v_exp_f32_e32 v124, v64
	global_load_dwordx2 v[64:65], v[60:61], off
	global_load_dwordx2 v[62:63], v[60:61], off offset:32
	s_waitcnt lgkmcnt(0)
	v_pk_add_f32 v[122:123], v[202:203], v[122:123]
	v_add_f32_e32 v124, 1.0, v124
	v_rcp_f32_e32 v152, v124
	s_waitcnt vmcnt(13)
	v_lshlrev_b32_e32 v126, 16, v67
	v_and_b32_e32 v127, 0xffff0000, v67
	s_waitcnt vmcnt(12)
	v_lshlrev_b32_e32 v130, 16, v69
	v_and_b32_e32 v131, 0xffff0000, v69
	s_waitcnt vmcnt(11)
	v_lshlrev_b32_e32 v134, 16, v71
	v_and_b32_e32 v135, 0xffff0000, v71
	s_waitcnt vmcnt(9)
	v_lshlrev_b32_e32 v140, 16, v109
	v_and_b32_e32 v141, 0xffff0000, v109
	s_waitcnt vmcnt(8)
	v_lshlrev_b32_e32 v144, 16, v107
	v_and_b32_e32 v145, 0xffff0000, v107
	s_waitcnt vmcnt(7)
	v_lshlrev_b32_e32 v148, 16, v73
	v_and_b32_e32 v149, 0xffff0000, v73
	v_lshlrev_b32_e32 v132, 16, v70
	v_and_b32_e32 v133, 0xffff0000, v70
	v_lshlrev_b32_e32 v146, 16, v72
	v_and_b32_e32 v147, 0xffff0000, v72
	s_waitcnt vmcnt(4)
	v_lshlrev_b32_e32 v72, 16, v120
	v_and_b32_e32 v73, 0xffff0000, v120
	v_lshlrev_b32_e32 v70, 16, v121
	v_and_b32_e32 v71, 0xffff0000, v121
	v_pk_add_f32 v[120:121], v[126:127], v[140:141]
	v_pk_add_f32 v[126:127], v[130:131], v[144:145]
	v_pk_add_f32 v[130:131], v[134:135], v[148:149]
	ds_bpermute_b32 v135, v231, v123
	ds_bpermute_b32 v134, v231, v122
	v_lshlrev_b32_e32 v136, 16, v110
	v_and_b32_e32 v137, 0xffff0000, v110
	v_lshlrev_b32_e32 v110, 16, v111
	v_and_b32_e32 v111, 0xffff0000, v111
	v_lshlrev_b32_e32 v150, 16, v112
	v_and_b32_e32 v151, 0xffff0000, v112
	v_lshlrev_b32_e32 v112, 16, v113
	v_and_b32_e32 v113, 0xffff0000, v113
	v_lshlrev_b32_e32 v124, 16, v66
	v_and_b32_e32 v125, 0xffff0000, v66
	v_lshlrev_b32_e32 v128, 16, v68
	v_and_b32_e32 v129, 0xffff0000, v68
	s_waitcnt vmcnt(3)
	v_lshlrev_b32_e32 v68, 16, v114
	v_and_b32_e32 v69, 0xffff0000, v114
	v_lshlrev_b32_e32 v66, 16, v115
	v_pk_add_f32 v[112:113], v[110:111], v[112:113]
	v_and_b32_e32 v67, 0xffff0000, v115
	s_waitcnt vmcnt(2)
	v_lshlrev_b32_e32 v114, 16, v116
	v_and_b32_e32 v115, 0xffff0000, v116
	v_lshlrev_b32_e32 v110, 16, v117
	s_waitcnt lgkmcnt(0)
	v_pk_add_f32 v[122:123], v[122:123], v[134:135]
	v_and_b32_e32 v111, 0xffff0000, v117
	global_load_dwordx2 v[116:117], v[60:61], off offset:64
	global_load_dwordx2 v[134:135], v[60:61], off offset:96
	v_lshlrev_b32_e32 v138, 16, v108
	v_and_b32_e32 v139, 0xffff0000, v108
	v_lshlrev_b32_e32 v142, 16, v106
	v_and_b32_e32 v143, 0xffff0000, v106
	v_lshlrev_b32_e32 v108, 16, v118
	v_and_b32_e32 v109, 0xffff0000, v118
	v_lshlrev_b32_e32 v106, 16, v119
	v_and_b32_e32 v107, 0xffff0000, v119
	v_pk_add_f32 v[118:119], v[124:125], v[138:139]
	v_pk_add_f32 v[124:125], v[128:129], v[142:143]
	v_pk_add_f32 v[128:129], v[132:133], v[146:147]
	v_pk_add_f32 v[132:133], v[136:137], v[150:151]
	v_div_scale_f32 v136, s[0:1], v123, v123, 1.0
	v_rcp_f32_e32 v137, v136
	s_nop 0
	v_fma_f32 v138, -v136, v137, 1.0
	v_fmac_f32_e32 v137, v138, v137
	v_div_scale_f32 v138, vcc, 1.0, v123, 1.0
	v_mul_f32_e32 v139, v138, v137
	v_fma_f32 v140, -v136, v139, v138
	v_fmac_f32_e32 v139, v140, v137
	v_fma_f32 v136, -v136, v139, v138
	v_div_fmas_f32 v136, v136, v137, v139
	v_div_fixup_f32 v136, v136, v123, 1.0
	v_cmp_lt_f32_e32 vcc, 0, v123
	s_nop 1
	v_cndmask_b32_e32 v123, 0, v136, vcc
	v_mul_f32_e32 v136, v152, v123
	v_pk_fma_f32 v[96:97], v[96:97], v[136:137], v[130:131] op_sel_hi:[1,0,1]
	v_pk_fma_f32 v[94:95], v[94:95], v[136:137], v[128:129] op_sel_hi:[1,0,1]
	v_pk_fma_f32 v[104:105], v[104:105], v[136:137], v[120:121] op_sel_hi:[1,0,1]
	v_cvt_pk_bf16_f32 v94, v94, v95
	v_cvt_pk_bf16_f32 v95, v96, v97
	global_store_dwordx2 v[58:59], v[94:95], off offset:64
	v_div_scale_f32 v94, s[0:1], v122, v122, 1.0
	v_rcp_f32_e32 v95, v94
	v_pk_fma_f32 v[102:103], v[102:103], v[136:137], v[118:119] op_sel_hi:[1,0,1]
	v_pk_fma_f32 v[100:101], v[100:101], v[136:137], v[126:127] op_sel_hi:[1,0,1]
	v_pk_fma_f32 v[98:99], v[98:99], v[136:137], v[124:125] op_sel_hi:[1,0,1]
	v_pk_fma_f32 v[92:93], v[92:93], v[136:137], v[112:113] op_sel_hi:[1,0,1]
	v_pk_fma_f32 v[90:91], v[90:91], v[136:137], v[132:133] op_sel_hi:[1,0,1]
	v_cvt_pk_bf16_f32 v102, v102, v103
	v_cvt_pk_bf16_f32 v103, v104, v105
	v_cvt_pk_bf16_f32 v98, v98, v99
	v_cvt_pk_bf16_f32 v99, v100, v101
	v_cvt_pk_bf16_f32 v90, v90, v91
	v_cvt_pk_bf16_f32 v91, v92, v93
	global_store_dwordx2 v[58:59], v[102:103], off
	global_store_dwordx2 v[58:59], v[98:99], off offset:32
	global_store_dwordx2 v[58:59], v[90:91], off offset:96
	v_fma_f32 v58, -v94, v95, 1.0
	v_fmac_f32_e32 v95, v58, v95
	v_div_scale_f32 v58, vcc, 1.0, v122, 1.0
	v_mul_f32_e32 v59, v58, v95
	v_fma_f32 v90, -v94, v59, v58
	v_fmac_f32_e32 v59, v90, v95
	v_lshlrev_b32_e32 v90, 16, v163
	v_mul_f32_e32 v90, 0xbfb8aa3b, v90
	v_exp_f32_e32 v90, v90
	v_fma_f32 v58, -v94, v59, v58
	v_div_fmas_f32 v58, v58, v95, v59
	v_div_fixup_f32 v58, v58, v122, 1.0
	v_add_f32_e32 v59, 1.0, v90
	v_rcp_f32_e32 v59, v59
	v_cmp_lt_f32_e32 vcc, 0, v122
	s_waitcnt vmcnt(7)
;     ...
;     for (int unit = (uone >= 0 ? uone : c.bid); unit < (uone >= 0 ? uone + 1 : 2 * NU); unit += c.G) {
;         const int g = unit / NU, t0 = ((g == 0) ? (unit % NU) : (NU - 1 - unit % NU)) * TB, tw0 = t0 + wave * TW;
;         const bf16_t* Ksrc; size_t kstride; const bf16_t* Vsrc; size_t vstride; int qcol;
;         if (MODE == 0) { Ksrc = proj + PC_SK + g * 64; kstride = PLD; Vsrc = vtb + (size_t)(4 + g) * 64 * T; vstride = T; qcol = PC_SQ + g * 256; }
;         else if (MODE == 1) { Ksrc = proj + PC_KW + g * 64; kstride = PLD; Vsrc = vtb + (size_t)(2 + g) * 64 * T; vstride = T; qcol = PC_NQ + g * 256; }
;         else if (MODE == 2) { Ksrc = kcb + (size_t)g * 1024 * 64; kstride = 64; Vsrc = vctb + (size_t)g * 64 * 1024; vstride = 1024; qcol = PC_NQ + g * 256; }
;         else { Ksrc = proj + PC_KS + g * 64; kstride = PLD; Vsrc = vtb + (size_t)(0 + g) * 64 * T; vstride = T; qcol = PC_NQ + g * 256; }
;         bf16x8 Bq[NQ][2]; bf16_t graw[NQ]; float sinkv = 0.f;
; #pragma unroll
;         for (int qd = 0; qd < NQ; ++qd) { const bf16_t* qp = proj + (size_t)(tw0 + 4 * qd + (n >> 2)) * PLD + qcol + hr * 64 + 8 * q;
;             Bq[qd][0] = *(const bf16x8*)qp; Bq[qd][1] = *(const bf16x8*)(qp + 32);
;             graw[qd] = (MODE != 0) ? proj[(size_t)(tw0 + 4 * qd + (n >> 2)) * PLD + PC_GL + (MODE == 2 ? 0 : (MODE == 3 ? 8 : 16)) + g * 4 + hr] : (bf16_t)0; }
;         if (MODE == 0) sinkv = inptr(c, I_SINK)[layer * 8 + g * 4 + hr];
;         __syncthreads();
;         if (MODE == 3) {
;             if (c.tid < 8) need[c.tid] = 0u;
;             __syncthreads();
;             { const int tok = c.tid >> 3, w8 = c.tid & 7; const unsigned mw = selp((unsigned char*)sel, t0 + tok, g)[w8]; selm[tok * 8 + w8] = mw; atomicOr((unsigned*)&need[w8], mw); }
;             __syncthreads();
;             if (c.tid < 256) { const int j = c.tid; const unsigned wd = need[j >> 5];
;                 if ((wd >> (j & 31)) & 1u) { int pos = __popc(wd & ((1u << (j & 31)) - 1u)); for (int w2 = 0; w2 < (j >> 5); ++w2) pos += __popc(need[w2]); list[pos] = j; } }
;             if (c.tid == 0) { int cnt = 0; for (int w2 = 0; w2 < 8; ++w2) cnt += __popc(need[w2]); nlist[0] = cnt; }
;             __syncthreads();
;         }
;     ...
;             for (int dt = 0; dt < 4; ++dt) { const f32x4 o = O[qd][dt] * scale; const int col = hh * 64 + 16 * dt + 4 * q;
	v_lshlrev_b32_e32 v90, 16, v64
	v_and_b32_e32 v91, 0xffff0000, v64
	v_cndmask_b32_e32 v58, 0, v58, vcc
	v_lshlrev_b32_e32 v64, 16, v65
	v_and_b32_e32 v65, 0xffff0000, v65
	v_mul_f32_e32 v58, v59, v58
	v_pk_add_f32 v[90:91], v[108:109], v[90:91]
	v_pk_add_f32 v[64:65], v[106:107], v[64:65]
	v_pk_fma_f32 v[86:87], v[86:87], v[58:59], v[90:91] op_sel_hi:[1,0,1]
	v_pk_fma_f32 v[64:65], v[88:89], v[58:59], v[64:65] op_sel_hi:[1,0,1]
	v_cvt_pk_bf16_f32 v86, v86, v87
	v_cvt_pk_bf16_f32 v87, v64, v65
	s_waitcnt vmcnt(6)
	v_lshlrev_b32_e32 v64, 16, v62
	v_and_b32_e32 v65, 0xffff0000, v62
	v_lshlrev_b32_e32 v62, 16, v63
	v_and_b32_e32 v63, 0xffff0000, v63
	v_pk_add_f32 v[64:65], v[72:73], v[64:65]
	v_pk_add_f32 v[62:63], v[70:71], v[62:63]
	v_pk_fma_f32 v[64:65], v[82:83], v[58:59], v[64:65] op_sel_hi:[1,0,1]
	v_pk_fma_f32 v[62:63], v[84:85], v[58:59], v[62:63] op_sel_hi:[1,0,1]
	v_cvt_pk_bf16_f32 v64, v64, v65
	v_cvt_pk_bf16_f32 v65, v62, v63
	global_store_dwordx2 v[60:61], v[64:65], off offset:32
	s_waitcnt vmcnt(6)
	v_lshlrev_b32_e32 v62, 16, v116
	v_and_b32_e32 v63, 0xffff0000, v116
	v_lshlrev_b32_e32 v64, 16, v117
	v_and_b32_e32 v65, 0xffff0000, v117
	v_pk_add_f32 v[62:63], v[68:69], v[62:63]
	v_pk_add_f32 v[64:65], v[66:67], v[64:65]
	v_pk_fma_f32 v[62:63], v[78:79], v[58:59], v[62:63] op_sel_hi:[1,0,1]
	v_pk_fma_f32 v[64:65], v[80:81], v[58:59], v[64:65] op_sel_hi:[1,0,1]
	v_cvt_pk_bf16_f32 v62, v62, v63
	v_cvt_pk_bf16_f32 v63, v64, v65
	global_store_dwordx2 v[60:61], v[62:63], off offset:64
	s_waitcnt vmcnt(6)
	v_lshlrev_b32_e32 v62, 16, v134
	v_and_b32_e32 v63, 0xffff0000, v134
	v_lshlrev_b32_e32 v64, 16, v135
	v_and_b32_e32 v65, 0xffff0000, v135
	v_pk_add_f32 v[62:63], v[114:115], v[62:63]
	v_pk_add_f32 v[64:65], v[110:111], v[64:65]
	global_store_dwordx2 v[60:61], v[86:87], off
	v_pk_fma_f32 v[64:65], v[76:77], v[58:59], v[64:65] op_sel_hi:[1,0,1]
	v_pk_fma_f32 v[58:59], v[74:75], v[58:59], v[62:63] op_sel_hi:[1,0,1]
	s_nop 0
	v_cvt_pk_bf16_f32 v58, v58, v59
	v_cvt_pk_bf16_f32 v59, v64, v65
	global_store_dwordx2 v[60:61], v[58:59], off offset:96
	s_and_saveexec_b64 s[0:1], s[8:9]
	v_add_u32_e32 v250, 0x100, v188
	v_mov_b32_e32 v186, 0x26400
	ds_write_b32 v186, v250
	s_or_b64 exec, exec, s[0:1]
	s_waitcnt lgkmcnt(0)
	s_barrier
	v_mov_b32_e32 v186, 0x26400
	ds_read_b32 v250, v186
	s_waitcnt lgkmcnt(0)
	v_readfirstlane_b32 s20, v250
	s_cmpk_gt_i32 s20, 0x1ff
	s_cbranch_scc1 .LBB0_1310
.LBB0_1121:
	s_and_b32 s0, s20, 1
	s_lshr_b32 s1, s20, 1
	s_sub_i32 s1, 0xff, s1
	s_lshl_b32 s1, s1, 6
	s_add_i32 s22, s1, s21
	v_or_b32_e32 v196, s22, v155
	s_lshl_b32 s2, s0, 8
	s_lshl_b32 s12, s0, 2
	v_ashrrev_i32_e32 v197, 31, v196
	s_ashr_i32 s3, s2, 31
	s_ashr_i32 s13, s12, 31
	v_lshlrev_b64 v[58:59], 13, v[196:197]
	v_or_b32_e32 v184, 4, v196
	v_lshl_add_u64 v[66:67], s[80:81], 0, v[58:59]
	s_lshl_b64 s[2:3], s[2:3], 1
	s_lshl_b64 s[4:5], s[12:13], 1
	v_ashrrev_i32_e32 v185, 31, v184
	v_lshl_add_u64 v[58:59], v[66:67], 0, s[2:3]
	v_lshl_add_u64 v[66:67], v[66:67], 0, s[4:5]
	v_mov_b32_e32 v165, v1
	v_lshlrev_b64 v[68:69], 13, v[184:185]
	v_lshl_add_u64 v[66:67], v[66:67], 0, v[164:165]
	v_lshl_add_u64 v[70:71], s[80:81], 0, v[68:69]
	v_add_co_u32_e32 v66, vcc, s97, v66
	v_lshl_add_u64 v[68:69], v[70:71], 0, s[2:3]
	v_lshl_add_u64 v[70:71], v[70:71], 0, s[4:5]
	v_lshl_add_u64 v[58:59], v[58:59], 0, v[0:1]
	v_mov_b32_e32 v163, v1
	v_addc_co_u32_e32 v67, vcc, 0, v67, vcc
	v_lshl_add_u64 v[68:69], v[68:69], 0, v[0:1]
	v_lshl_add_u64 v[70:71], v[70:71], 0, v[164:165]
	v_lshl_add_u64 v[62:63], v[58:59], 0, v[162:163]
	v_lshl_add_u64 v[72:73], v[68:69], 0, v[162:163]
	v_add_co_u32_e32 v74, vcc, 0x1000, v70
	global_load_dwordx4 v[58:61], v[62:63], off offset:3584
	s_nop 0
	global_load_dwordx4 v[62:65], v[62:63], off offset:3648
	s_nop 0
	global_load_ushort v235, v[66:67], off offset:2064
	s_nop 0
	global_load_dwordx4 v[66:69], v[72:73], off offset:3584
	v_addc_co_u32_e32 v75, vcc, 0, v71, vcc
	global_load_dwordx4 v[70:73], v[72:73], off offset:3648
	s_nop 0
	global_load_ushort v163, v[74:75], off offset:2064
	s_waitcnt lgkmcnt(0)
	s_barrier
	s_and_saveexec_b64 s[2:3], s[38:39]
	ds_write_b32 v225, v1
	s_or_b64 exec, exec, s[2:3]
	v_add_u32_e32 v74, s1, v221
	v_ashrrev_i32_e32 v75, 31, v74
	v_lshlrev_b64 v[74:75], 13, v[74:75]
	s_lshl_b32 s2, s0, 5
	v_lshl_add_u64 v[74:75], s[76:77], 0, v[74:75]
	s_ashr_i32 s3, s2, 31
	v_lshl_add_u64 v[74:75], v[74:75], 0, s[2:3]
	v_mov_b32_e32 v167, v1
	v_lshl_add_u64 v[74:75], v[74:75], 0, v[166:167]
	v_add_co_u32_e32 v74, vcc, 0x7f01000, v74
	s_waitcnt lgkmcnt(0)
	s_nop 0
	v_addc_co_u32_e32 v75, vcc, 0, v75, vcc
	s_barrier
	global_load_dword v74, v[74:75], off offset:2176
	s_waitcnt vmcnt(0)
	ds_write_b32 v222, v74
	ds_or_b32 v223, v74
	s_waitcnt lgkmcnt(0)
	s_barrier
	s_and_saveexec_b64 s[2:3], s[6:7]
	s_cbranch_execz .LBB0_1138
	v_readlane_b32 s1, v253, 33
	v_lshlrev_b32_e64 v75, v154, 1
	s_nop 0
	v_lshl_add_u32 v74, v226, 2, s1
	ds_read_b32 v74, v74
	s_waitcnt lgkmcnt(0)
	v_and_b32_e32 v75, v74, v75
	v_cmp_ne_u32_e32 vcc, 0, v75
	s_and_b64 exec, exec, vcc
	s_cbranch_execz .LBB0_1138
	v_and_b32_e32 v74, v74, v227
	v_bcnt_u32_b32 v74, v74, 0
	s_and_saveexec_b64 s[4:5], s[46:47]
	s_cbranch_execz .LBB0_1137
	s_mov_b64 s[16:17], -1
	v_mov_b32_e32 v75, 0
	s_and_saveexec_b64 s[14:15], s[48:49]
	s_cbranch_execz .LBB0_1132
	v_mov_b32_e32 v75, 0
	s_mov_b64 s[16:17], 0
	v_mov_b32_e32 v76, 0
	v_mov_b32_e32 v77, 0
	v_readlane_b32 s1, v253, 34
	v_mov_b32_e32 v78, v232
